# v15
# baseline (speedup 1.0000x reference)
.LBB0_26:
	s_or_b64 exec, exec, s[10:11]
	s_waitcnt vmcnt(1)
	v_cmp_lt_i32_e64 s[16:17], -1, v14
	v_lshrrev_b32_e32 v35, 6, v14
	s_and_saveexec_b64 s[4:5], s[16:17]
	v_and_b32_e32 v20, 0x3fffffc, v35
	v_mov_b32_e32 v21, 1
	ds_add_rtn_u32 v20, v20, v21 offset:25024
	s_or_b64 exec, exec, s[4:5]
	v_cmp_lt_i32_e64 s[14:15], -1, v15
	v_mov_b32_e32 v23, 0
	v_lshrrev_b32_e32 v34, 6, v15
	v_mov_b32_e32 v33, 0
	s_and_saveexec_b64 s[4:5], s[14:15]
	v_and_b32_e32 v21, 0x3fffffc, v34
	v_mov_b32_e32 v22, 1
	ds_add_rtn_u32 v33, v21, v22 offset:25024
	s_or_b64 exec, exec, s[4:5]
	v_cmp_lt_i32_e64 s[12:13], -1, v16
	v_lshrrev_b32_e32 v32, 6, v16
	s_and_saveexec_b64 s[4:5], s[12:13]
	v_and_b32_e32 v21, 0x3fffffc, v32
	v_mov_b32_e32 v22, 1
	ds_add_rtn_u32 v23, v21, v22 offset:25024
	s_or_b64 exec, exec, s[4:5]
	v_cmp_lt_i32_e64 s[10:11], -1, v17
	v_mov_b32_e32 v22, 0
	v_lshrrev_b32_e32 v31, 6, v17
	v_mov_b32_e32 v30, 0
	s_and_saveexec_b64 s[4:5], s[10:11]
	v_and_b32_e32 v21, 0x3fffffc, v31
	v_mov_b32_e32 v24, 1
	ds_add_rtn_u32 v30, v21, v24 offset:25024
	s_or_b64 exec, exec, s[4:5]
	v_cmp_lt_i32_e64 s[8:9], -1, v2
	v_lshrrev_b32_e32 v29, 6, v2
	s_and_saveexec_b64 s[4:5], s[8:9]
	v_and_b32_e32 v21, 0x3fffffc, v29
	v_mov_b32_e32 v22, 1
	ds_add_rtn_u32 v22, v21, v22 offset:25024
	s_or_b64 exec, exec, s[4:5]
	v_cmp_lt_i32_e64 s[6:7], -1, v3
	v_mov_b32_e32 v21, 0
	v_lshrrev_b32_e32 v28, 6, v3
	v_mov_b32_e32 v27, 0
	s_and_saveexec_b64 s[4:5], s[6:7]
	v_and_b32_e32 v24, 0x3fffffc, v28
	v_mov_b32_e32 v25, 1
	ds_add_rtn_u32 v27, v24, v25 offset:25024
	s_or_b64 exec, exec, s[4:5]
	v_cmp_lt_i32_e64 s[4:5], -1, v4
	v_lshrrev_b32_e32 v26, 6, v4
	s_and_saveexec_b64 s[18:19], s[4:5]
	v_and_b32_e32 v21, 0x3fffffc, v26
	v_mov_b32_e32 v24, 1
	ds_add_rtn_u32 v21, v21, v24 offset:25024
	s_or_b64 exec, exec, s[18:19]
	v_cmp_lt_i32_e64 s[18:19], -1, v5
	v_mov_b32_e32 v36, 0
	v_lshrrev_b32_e32 v25, 6, v5
	v_mov_b32_e32 v24, 0
	s_and_saveexec_b64 s[20:21], s[18:19]
	v_and_b32_e32 v24, 0x3fffffc, v25
	v_mov_b32_e32 v37, 1
	ds_add_rtn_u32 v24, v24, v37 offset:25024
	s_or_b64 exec, exec, s[20:21]
	s_waitcnt lgkmcnt(0)
	s_barrier
	s_and_saveexec_b64 s[20:21], vcc
	ds_read_b32 v36, v19 offset:25024
	s_or_b64 exec, exec, s[20:21]
	v_and_b32_e32 v41, 63, v0
	v_lshrrev_b32_e32 v40, 6, v0
	s_waitcnt lgkmcnt(0)
	v_mov_b32_e32 v37, v36
	v_mov_b32_e32 v38, 0
	s_nop 1
	v_add_u32_dpp v37, v37, v37 row_shr:1 row_mask:0xf bank_mask:0xf bound_ctrl:1
	s_nop 1
	v_add_u32_dpp v37, v37, v37 row_shr:2 row_mask:0xf bank_mask:0xf bound_ctrl:1
	s_nop 1
	v_add_u32_dpp v37, v37, v37 row_shr:4 row_mask:0xf bank_mask:0xf bound_ctrl:1
	s_nop 1
	v_add_u32_dpp v37, v37, v37 row_shr:8 row_mask:0xf bank_mask:0xf bound_ctrl:1
	s_nop 1
	v_add_u32_dpp v37, v37, v37 row_bcast:15 row_mask:0xa bank_mask:0xf
	s_nop 1
	v_add_u32_dpp v37, v37, v37 row_bcast:31 row_mask:0xc bank_mask:0xf
	v_cmp_eq_u32_e64 s[20:21], 63, v41
	s_and_saveexec_b64 s[22:23], s[20:21]
	v_lshlrev_b32_e32 v38, 2, v40
	ds_write_b32 v38, v37 offset:27072
	s_or_b64 exec, exec, s[22:23]
	s_load_dwordx4 s[20:23], s[0:1], 0x58
	v_cmp_lt_u32_e64 s[0:1], 63, v0
	v_mov_b32_e32 v38, 0
	s_waitcnt lgkmcnt(0)
	s_barrier
	s_and_saveexec_b64 s[26:27], s[0:1]
	s_cbranch_execz .LBB0_56
	v_add_u32_e32 v38, -1, v40
	v_cmp_lt_u32_e64 s[0:1], 6, v38
	v_mov_b32_e32 v38, 0
	v_mov_b32_e32 v39, 0
	s_and_saveexec_b64 s[28:29], s[0:1]
	s_cbranch_execz .LBB0_51
	v_and_b32_e32 v39, 8, v40
	s_mov_b32 s3, 0
	s_movk_i32 s33, 0x69c0
	s_mov_b64 s[30:31], 0
	v_mov_b32_e32 v38, 0

.LBB1_68:
	s_or_b64 exec, exec, s[26:27]
	v_mov_b32_e32 v2, 0
	s_waitcnt lgkmcnt(0)
	s_barrier
	s_and_saveexec_b64 s[18:19], vcc
	v_lshlrev_b32_e32 v2, 2, v0
	ds_read_b32 v2, v2 offset:26624
	s_or_b64 exec, exec, s[18:19]
	s_waitcnt lgkmcnt(0)
	v_mov_b32_e32 v3, v2
	v_mov_b32_e32 v16, 0
	s_nop 1
	v_add_u32_dpp v3, v3, v3 row_shr:1 row_mask:0xf bank_mask:0xf bound_ctrl:1
	s_nop 1
	v_add_u32_dpp v3, v3, v3 row_shr:2 row_mask:0xf bank_mask:0xf bound_ctrl:1
	s_nop 1
	v_add_u32_dpp v3, v3, v3 row_shr:4 row_mask:0xf bank_mask:0xf bound_ctrl:1
	s_nop 1
	v_add_u32_dpp v3, v3, v3 row_shr:8 row_mask:0xf bank_mask:0xf bound_ctrl:1
	s_nop 1
	v_add_u32_dpp v3, v3, v3 row_bcast:15 row_mask:0xa bank_mask:0xf
	s_nop 1
	v_add_u32_dpp v3, v3, v3 row_bcast:31 row_mask:0xc bank_mask:0xf
	v_lshrrev_b32_e32 v17, 6, v0
	v_cmp_eq_u32_e64 s[18:19], 63, v14
	s_and_saveexec_b64 s[26:27], s[18:19]
	v_lshlrev_b32_e32 v14, 2, v17
	ds_write_b32 v14, v3 offset:27648
	s_or_b64 exec, exec, s[26:27]
	v_cmp_lt_u32_e64 s[18:19], 63, v0
	v_mov_b32_e32 v14, 0
	s_waitcnt lgkmcnt(0)
	s_barrier
	s_and_saveexec_b64 s[26:27], s[18:19]
	s_cbranch_execz .LBB1_82
	v_add_u32_e32 v14, -1, v17
	v_cmp_lt_u32_e64 s[18:19], 6, v14
	v_mov_b32_e32 v14, 0
	v_mov_b32_e32 v16, 0
	s_and_saveexec_b64 s[28:29], s[18:19]
	s_cbranch_execz .LBB1_77
	v_and_b32_e32 v16, 8, v17
	s_mov_b32 s3, 0
	s_movk_i32 s33, 0x6c00
	s_mov_b64 s[30:31], 0
	v_mov_b32_e32 v14, 0

.LBB1_186:
	s_endpgm
	s_nop 0
	s_nop 0
	s_nop 0
	s_nop 0
	s_nop 0
	s_nop 0
	s_nop 0
	s_nop 0
	s_nop 0
	s_nop 0
	s_nop 0
	s_nop 0
	s_nop 0
	s_nop 0
	s_nop 0
	s_endpgm
